# v81 + B-fragment LDS addresses via ds_read offsets in the in-projection, FFN-up, gates and merge K-loops (64 VALU per iteration set removed)
# speedup vs baseline: 1.0093x; 1.0045x over previous
.LBB0_850:
	s_add_u32 s54, s54, 0x20080
	s_addc_u32 s55, s55, 0
	s_add_u32 s29, s56, 0x100
	s_addc_u32 s39, s57, 0
	s_mov_b32 s41, -2
	v_add_u32_e32 v0, 0x10000, v237
.LBB0_851:
	ds_read_b128 v[130:133], v0
	ds_read_b128 v[134:137], v0 offset:1024
	ds_read_b128 v[138:141], v0 offset:2048
	ds_read_b128 v[142:145], v0 offset:3072
	ds_read_b128 v[146:149], v0 offset:16384
	ds_read_b128 v[150:153], v0 offset:17408
	ds_read_b128 v[154:157], v0 offset:18432
	ds_read_b128 v[158:161], v0 offset:19456
	s_add_u32 s43, s54, 0xfffe0080
	s_addc_u32 s45, s55, -1
	s_cmp_eq_u32 s41, 4
	s_cselect_b32 s59, s49, s45
	s_cselect_b32 s58, s48, s43
	s_cselect_b32 s57, s51, s39
	s_cselect_b32 s56, s50, s29
	s_add_i32 m0, s61, 0xc000
	ds_read_b128 v[162:165], v236
	ds_read_b128 v[166:169], v236 offset:1024
	ds_read_b128 v[170:173], v236 offset:2048
	ds_read_b128 v[174:177], v236 offset:3072
	ds_read_b128 v[178:181], v236 offset:4096
	ds_read_b128 v[182:185], v236 offset:5120
	ds_read_b128 v[186:189], v236 offset:6144
	ds_read_b128 v[190:193], v236 offset:7168
	global_load_lds_dwordx4 v206, s[54:55]
	s_add_i32 m0, s61, 0xe000
	s_nop 0
	global_load_lds_dwordx4 v208, s[54:55]
	s_waitcnt vmcnt(8)
	s_waitcnt lgkmcnt(0)
	s_barrier
	s_setprio 1
	s_waitcnt lgkmcnt(0)
	v_mfma_f32_16x16x32_bf16 v[126:129], v[130:133], v[162:165], v[126:129]
	v_mfma_f32_16x16x32_bf16 v[122:125], v[138:141], v[162:165], v[122:125]
	v_mfma_f32_16x16x32_bf16 v[118:121], v[130:133], v[170:173], v[118:121]
	v_mfma_f32_16x16x32_bf16 v[114:117], v[138:141], v[170:173], v[114:117]
	v_mfma_f32_16x16x32_bf16 v[110:113], v[130:133], v[178:181], v[110:113]
	v_mfma_f32_16x16x32_bf16 v[106:109], v[138:141], v[178:181], v[106:109]
	v_mfma_f32_16x16x32_bf16 v[102:105], v[130:133], v[186:189], v[102:105]
	v_mfma_f32_16x16x32_bf16 v[98:101], v[138:141], v[186:189], v[98:101]
	v_mfma_f32_16x16x32_bf16 v[126:129], v[134:137], v[166:169], v[126:129]
	v_mfma_f32_16x16x32_bf16 v[122:125], v[142:145], v[166:169], v[122:125]
	v_mfma_f32_16x16x32_bf16 v[118:121], v[134:137], v[174:177], v[118:121]
	v_mfma_f32_16x16x32_bf16 v[114:117], v[142:145], v[174:177], v[114:117]
	v_mfma_f32_16x16x32_bf16 v[110:113], v[134:137], v[182:185], v[110:113]
	v_mfma_f32_16x16x32_bf16 v[106:109], v[142:145], v[182:185], v[106:109]
	v_mfma_f32_16x16x32_bf16 v[102:105], v[134:137], v[190:193], v[102:105]
	v_mfma_f32_16x16x32_bf16 v[98:101], v[142:145], v[190:193], v[98:101]
	s_setprio 0
	s_setprio 1
	v_mfma_f32_16x16x32_bf16 v[94:97], v[146:149], v[162:165], v[94:97]
	v_mfma_f32_16x16x32_bf16 v[90:93], v[154:157], v[162:165], v[90:93]
	v_mfma_f32_16x16x32_bf16 v[86:89], v[146:149], v[170:173], v[86:89]
	v_mfma_f32_16x16x32_bf16 v[82:85], v[154:157], v[170:173], v[82:85]
	v_mfma_f32_16x16x32_bf16 v[78:81], v[146:149], v[178:181], v[78:81]
	v_mfma_f32_16x16x32_bf16 v[74:77], v[154:157], v[178:181], v[74:77]
	v_mfma_f32_16x16x32_bf16 v[70:73], v[146:149], v[186:189], v[70:73]
	v_mfma_f32_16x16x32_bf16 v[66:69], v[154:157], v[186:189], v[66:69]
	v_mfma_f32_16x16x32_bf16 v[94:97], v[150:153], v[166:169], v[94:97]
	v_mfma_f32_16x16x32_bf16 v[90:93], v[158:161], v[166:169], v[90:93]
	v_mfma_f32_16x16x32_bf16 v[86:89], v[150:153], v[174:177], v[86:89]
	v_mfma_f32_16x16x32_bf16 v[82:85], v[158:161], v[174:177], v[82:85]
	v_mfma_f32_16x16x32_bf16 v[78:81], v[150:153], v[182:185], v[78:81]
	v_mfma_f32_16x16x32_bf16 v[74:77], v[158:161], v[182:185], v[74:77]
	v_mfma_f32_16x16x32_bf16 v[70:73], v[150:153], v[190:193], v[70:73]
	v_mfma_f32_16x16x32_bf16 v[66:69], v[158:161], v[190:193], v[66:69]
	s_setprio 0
	s_barrier
	s_mov_b32 m0, s62
	v_lshl_add_u64 v[210:211], s[56:57], 0, v[200:201]
	s_add_u32 vcc_lo, s56, 0x20000
	ds_read_b128 v[162:165], v236 offset:16384
	ds_read_b128 v[166:169], v236 offset:17408
	ds_read_b128 v[170:173], v236 offset:18432
	ds_read_b128 v[174:177], v236 offset:19456
	ds_read_b128 v[178:181], v236 offset:20480
	ds_read_b128 v[182:185], v236 offset:21504
	ds_read_b128 v[186:189], v236 offset:22528
	ds_read_b128 v[190:193], v236 offset:23552
	global_load_lds_dwordx4 v200, s[56:57]
	v_lshl_add_u64 v[212:213], s[56:57], 0, v[204:205]
	s_mov_b32 m0, s63
	s_addc_u32 vcc_hi, s57, 0
	global_load_lds_dwordx4 v204, s[56:57]
	v_lshl_add_u64 v[214:215], vcc, 0, v[200:201]
	s_mov_b32 m0, s64
	v_lshl_add_u64 v[216:217], s[58:59], 0, v[202:203]
	global_load_lds_dwordx4 v200, vcc
	v_lshl_add_u64 v[214:215], vcc, 0, v[204:205]
	s_mov_b32 m0, s65
	s_nop 0
	global_load_lds_dwordx4 v204, vcc
	v_lshl_add_u64 v[214:215], s[58:59], 0, v[194:195]
	s_mov_b32 m0, s61
	s_nop 0
	global_load_lds_dwordx4 v194, s[58:59]
	s_mov_b32 m0, s66
	s_nop 0
	global_load_lds_dwordx4 v202, s[58:59]
	s_waitcnt vmcnt(8)
	s_waitcnt lgkmcnt(0)
	s_barrier
	s_setprio 1
	s_waitcnt lgkmcnt(0)
	v_mfma_f32_16x16x32_bf16 v[62:65], v[130:133], v[162:165], v[62:65]
	v_mfma_f32_16x16x32_bf16 v[58:61], v[138:141], v[162:165], v[58:61]
	v_mfma_f32_16x16x32_bf16 v[54:57], v[130:133], v[170:173], v[54:57]
	v_mfma_f32_16x16x32_bf16 v[50:53], v[138:141], v[170:173], v[50:53]
	v_mfma_f32_16x16x32_bf16 v[46:49], v[130:133], v[178:181], v[46:49]
	v_mfma_f32_16x16x32_bf16 v[42:45], v[138:141], v[178:181], v[42:45]
	v_mfma_f32_16x16x32_bf16 v[38:41], v[130:133], v[186:189], v[38:41]
	v_mfma_f32_16x16x32_bf16 v[34:37], v[138:141], v[186:189], v[34:37]
	v_mfma_f32_16x16x32_bf16 v[62:65], v[134:137], v[166:169], v[62:65]
	v_mfma_f32_16x16x32_bf16 v[58:61], v[142:145], v[166:169], v[58:61]
	v_mfma_f32_16x16x32_bf16 v[54:57], v[134:137], v[174:177], v[54:57]
	v_mfma_f32_16x16x32_bf16 v[50:53], v[142:145], v[174:177], v[50:53]
	v_mfma_f32_16x16x32_bf16 v[46:49], v[134:137], v[182:185], v[46:49]
	v_mfma_f32_16x16x32_bf16 v[42:45], v[142:145], v[182:185], v[42:45]
	v_mfma_f32_16x16x32_bf16 v[38:41], v[134:137], v[190:193], v[38:41]
	v_mfma_f32_16x16x32_bf16 v[34:37], v[142:145], v[190:193], v[34:37]
	s_setprio 0
	s_setprio 1
	v_mfma_f32_16x16x32_bf16 v[30:33], v[146:149], v[162:165], v[30:33]
	v_mfma_f32_16x16x32_bf16 v[26:29], v[154:157], v[162:165], v[26:29]
	v_mfma_f32_16x16x32_bf16 v[22:25], v[146:149], v[170:173], v[22:25]
	v_mfma_f32_16x16x32_bf16 v[18:21], v[154:157], v[170:173], v[18:21]
	v_mfma_f32_16x16x32_bf16 v[14:17], v[146:149], v[178:181], v[14:17]
	v_mfma_f32_16x16x32_bf16 v[10:13], v[154:157], v[178:181], v[10:13]
	v_mfma_f32_16x16x32_bf16 v[6:9], v[146:149], v[186:189], v[6:9]
	v_mfma_f32_16x16x32_bf16 v[2:5], v[154:157], v[186:189], v[2:5]
	v_mfma_f32_16x16x32_bf16 v[30:33], v[150:153], v[166:169], v[30:33]
	v_mfma_f32_16x16x32_bf16 v[26:29], v[158:161], v[166:169], v[26:29]
	v_mfma_f32_16x16x32_bf16 v[22:25], v[150:153], v[174:177], v[22:25]
	v_mfma_f32_16x16x32_bf16 v[18:21], v[158:161], v[174:177], v[18:21]
	v_mfma_f32_16x16x32_bf16 v[14:17], v[150:153], v[182:185], v[14:17]
	v_mfma_f32_16x16x32_bf16 v[10:13], v[158:161], v[182:185], v[10:13]
	v_mfma_f32_16x16x32_bf16 v[6:9], v[150:153], v[190:193], v[6:9]
	v_mfma_f32_16x16x32_bf16 v[2:5], v[158:161], v[190:193], v[2:5]
	s_setprio 0
	s_barrier
	ds_read_b128 v[130:133], v0 offset:32768
	ds_read_b128 v[134:137], v0 offset:33792
	ds_read_b128 v[138:141], v0 offset:34816
	ds_read_b128 v[142:145], v0 offset:35840
	ds_read_b128 v[146:149], v0 offset:49152
	ds_read_b128 v[150:153], v0 offset:50176
	ds_read_b128 v[154:157], v0 offset:51200
	ds_read_b128 v[158:161], v0 offset:52224
	s_add_u32 s58, s58, 0x20000
	s_addc_u32 s59, s59, 0
	s_mov_b32 m0, s67
	v_lshl_add_u64 v[218:219], s[58:59], 0, v[194:195]
	ds_read_b128 v[162:165], v236 offset:32768
	ds_read_b128 v[166:169], v236 offset:33792
	ds_read_b128 v[170:173], v236 offset:34816
	ds_read_b128 v[174:177], v236 offset:35840
	ds_read_b128 v[178:181], v236 offset:36864
	ds_read_b128 v[182:185], v236 offset:37888
	ds_read_b128 v[186:189], v236 offset:38912
	ds_read_b128 v[190:193], v236 offset:39936
	global_load_lds_dwordx4 v194, s[58:59]
	v_lshl_add_u64 v[218:219], s[58:59], 0, v[202:203]
	s_mov_b32 m0, s82
	s_nop 0
	global_load_lds_dwordx4 v202, s[58:59]
	s_waitcnt vmcnt(8)
	s_waitcnt lgkmcnt(0)
	s_barrier
	s_setprio 1
	s_waitcnt lgkmcnt(0)
	v_mfma_f32_16x16x32_bf16 v[126:129], v[130:133], v[162:165], v[126:129]
	v_mfma_f32_16x16x32_bf16 v[122:125], v[138:141], v[162:165], v[122:125]
	v_mfma_f32_16x16x32_bf16 v[118:121], v[130:133], v[170:173], v[118:121]
	v_mfma_f32_16x16x32_bf16 v[114:117], v[138:141], v[170:173], v[114:117]
	v_mfma_f32_16x16x32_bf16 v[110:113], v[130:133], v[178:181], v[110:113]
	v_mfma_f32_16x16x32_bf16 v[106:109], v[138:141], v[178:181], v[106:109]
	v_mfma_f32_16x16x32_bf16 v[102:105], v[130:133], v[186:189], v[102:105]
	v_mfma_f32_16x16x32_bf16 v[98:101], v[138:141], v[186:189], v[98:101]
	v_mfma_f32_16x16x32_bf16 v[126:129], v[134:137], v[166:169], v[126:129]
	v_mfma_f32_16x16x32_bf16 v[122:125], v[142:145], v[166:169], v[122:125]
	v_mfma_f32_16x16x32_bf16 v[118:121], v[134:137], v[174:177], v[118:121]
	v_mfma_f32_16x16x32_bf16 v[114:117], v[142:145], v[174:177], v[114:117]
	v_mfma_f32_16x16x32_bf16 v[110:113], v[134:137], v[182:185], v[110:113]
	v_mfma_f32_16x16x32_bf16 v[106:109], v[142:145], v[182:185], v[106:109]
	v_mfma_f32_16x16x32_bf16 v[102:105], v[134:137], v[190:193], v[102:105]
	v_mfma_f32_16x16x32_bf16 v[98:101], v[142:145], v[190:193], v[98:101]
	s_setprio 0
	s_setprio 1
	v_mfma_f32_16x16x32_bf16 v[94:97], v[146:149], v[162:165], v[94:97]
	v_mfma_f32_16x16x32_bf16 v[90:93], v[154:157], v[162:165], v[90:93]
	v_mfma_f32_16x16x32_bf16 v[86:89], v[146:149], v[170:173], v[86:89]
	v_mfma_f32_16x16x32_bf16 v[82:85], v[154:157], v[170:173], v[82:85]
	v_mfma_f32_16x16x32_bf16 v[78:81], v[146:149], v[178:181], v[78:81]
	v_mfma_f32_16x16x32_bf16 v[74:77], v[154:157], v[178:181], v[74:77]
	v_mfma_f32_16x16x32_bf16 v[70:73], v[146:149], v[186:189], v[70:73]
	v_mfma_f32_16x16x32_bf16 v[66:69], v[154:157], v[186:189], v[66:69]
	v_mfma_f32_16x16x32_bf16 v[94:97], v[150:153], v[166:169], v[94:97]
	v_mfma_f32_16x16x32_bf16 v[90:93], v[158:161], v[166:169], v[90:93]
	v_mfma_f32_16x16x32_bf16 v[86:89], v[150:153], v[174:177], v[86:89]
	v_mfma_f32_16x16x32_bf16 v[82:85], v[158:161], v[174:177], v[82:85]
	v_mfma_f32_16x16x32_bf16 v[78:81], v[150:153], v[182:185], v[78:81]
	v_mfma_f32_16x16x32_bf16 v[74:77], v[158:161], v[182:185], v[74:77]
	v_mfma_f32_16x16x32_bf16 v[70:73], v[150:153], v[190:193], v[70:73]
	v_mfma_f32_16x16x32_bf16 v[66:69], v[158:161], v[190:193], v[66:69]
	s_setprio 0
	s_barrier
	s_mov_b32 m0, s88
	v_lshl_add_u64 v[210:211], v[210:211], 0, s[18:19]
	s_add_u32 s56, s56, 0x20080
	ds_read_b128 v[162:165], v236 offset:49152
	ds_read_b128 v[166:169], v236 offset:50176
	ds_read_b128 v[170:173], v236 offset:51200
	ds_read_b128 v[174:177], v236 offset:52224
	ds_read_b128 v[178:181], v236 offset:53248
	ds_read_b128 v[182:185], v236 offset:54272
	ds_read_b128 v[186:189], v236 offset:55296
	ds_read_b128 v[190:193], v236 offset:56320
	global_load_lds_dwordx4 v[210:211], off
	v_lshl_add_u64 v[210:211], v[212:213], 0, s[18:19]
	s_mov_b32 m0, s89
	s_addc_u32 s57, s57, 0
	global_load_lds_dwordx4 v[210:211], off
	s_mov_b32 m0, s92
	s_nop 0
	global_load_lds_dwordx4 v200, s[56:57]
	s_mov_b32 m0, s93
	s_nop 0
	global_load_lds_dwordx4 v204, s[56:57]
	v_lshl_add_u64 v[210:211], v[214:215], 0, s[18:19]
	s_mov_b32 m0, s90
	s_nop 0
	global_load_lds_dwordx4 v[210:211], off
	v_lshl_add_u64 v[210:211], v[216:217], 0, s[18:19]
	s_mov_b32 m0, s91
	s_nop 0
	global_load_lds_dwordx4 v[210:211], off
	s_waitcnt vmcnt(8)
	s_waitcnt lgkmcnt(0)
	s_barrier
	s_setprio 1
	s_waitcnt lgkmcnt(0)
	v_mfma_f32_16x16x32_bf16 v[62:65], v[130:133], v[162:165], v[62:65]
	v_mfma_f32_16x16x32_bf16 v[58:61], v[138:141], v[162:165], v[58:61]
	v_mfma_f32_16x16x32_bf16 v[54:57], v[130:133], v[170:173], v[54:57]
	v_mfma_f32_16x16x32_bf16 v[50:53], v[138:141], v[170:173], v[50:53]
	v_mfma_f32_16x16x32_bf16 v[46:49], v[130:133], v[178:181], v[46:49]
	v_mfma_f32_16x16x32_bf16 v[42:45], v[138:141], v[178:181], v[42:45]
	v_mfma_f32_16x16x32_bf16 v[38:41], v[130:133], v[186:189], v[38:41]
	v_mfma_f32_16x16x32_bf16 v[34:37], v[138:141], v[186:189], v[34:37]
	v_mfma_f32_16x16x32_bf16 v[62:65], v[134:137], v[166:169], v[62:65]
	v_mfma_f32_16x16x32_bf16 v[58:61], v[142:145], v[166:169], v[58:61]
	v_mfma_f32_16x16x32_bf16 v[54:57], v[134:137], v[174:177], v[54:57]
	v_mfma_f32_16x16x32_bf16 v[50:53], v[142:145], v[174:177], v[50:53]
	v_mfma_f32_16x16x32_bf16 v[46:49], v[134:137], v[182:185], v[46:49]
	v_mfma_f32_16x16x32_bf16 v[42:45], v[142:145], v[182:185], v[42:45]
	v_mfma_f32_16x16x32_bf16 v[38:41], v[134:137], v[190:193], v[38:41]
	v_mfma_f32_16x16x32_bf16 v[34:37], v[142:145], v[190:193], v[34:37]
	s_setprio 0
	s_setprio 1
	v_mfma_f32_16x16x32_bf16 v[30:33], v[146:149], v[162:165], v[30:33]
	v_mfma_f32_16x16x32_bf16 v[26:29], v[154:157], v[162:165], v[26:29]
	v_mfma_f32_16x16x32_bf16 v[22:25], v[146:149], v[170:173], v[22:25]
	v_mfma_f32_16x16x32_bf16 v[18:21], v[154:157], v[170:173], v[18:21]
	v_mfma_f32_16x16x32_bf16 v[14:17], v[146:149], v[178:181], v[14:17]
	v_mfma_f32_16x16x32_bf16 v[10:13], v[154:157], v[178:181], v[10:13]
	v_mfma_f32_16x16x32_bf16 v[6:9], v[146:149], v[186:189], v[6:9]
	v_mfma_f32_16x16x32_bf16 v[2:5], v[154:157], v[186:189], v[2:5]
	v_mfma_f32_16x16x32_bf16 v[30:33], v[150:153], v[166:169], v[30:33]
	v_mfma_f32_16x16x32_bf16 v[26:29], v[158:161], v[166:169], v[26:29]
	v_mfma_f32_16x16x32_bf16 v[22:25], v[150:153], v[174:177], v[22:25]
	v_mfma_f32_16x16x32_bf16 v[18:21], v[158:161], v[174:177], v[18:21]
	v_mfma_f32_16x16x32_bf16 v[14:17], v[150:153], v[182:185], v[14:17]
	v_mfma_f32_16x16x32_bf16 v[10:13], v[158:161], v[182:185], v[10:13]
	v_mfma_f32_16x16x32_bf16 v[6:9], v[150:153], v[190:193], v[6:9]
	v_mfma_f32_16x16x32_bf16 v[2:5], v[158:161], v[190:193], v[2:5]
	s_setprio 0
	s_barrier
	s_add_i32 s41, s41, 2
	s_add_u32 s54, s54, 0x100
	s_addc_u32 s55, s55, 0
	s_add_u32 s29, s29, 0x100
	s_addc_u32 s39, s39, 0
	s_cmp_gt_u32 s41, 5
	s_cbranch_scc0 .LBB0_851
	s_and_b64 vcc, exec, s[16:17]
	s_cbranch_vccz .LBB0_854
	s_barrier

.LBB0_1057:
	s_ashr_i32 s39, s38, 31
	s_lshl_b64 s[42:43], s[38:39], 19
	v_readlane_b32 s44, v253, 34
	v_readlane_b32 s45, v253, 35
	s_add_u32 s42, s44, s42
	s_addc_u32 s43, s45, s43
	s_and_b64 s[44:45], s[46:47], exec
	s_cselect_b32 s29, s43, s37
	s_cselect_b32 s39, s42, s36
	s_ashr_i32 s41, s40, 31
	s_lshl_b64 s[44:45], s[40:41], 19
	s_add_u32 s44, s31, s44
	s_addc_u32 s45, s34, s45
	s_and_b64 s[50:51], s[46:47], exec
	s_cselect_b32 s41, s45, s49
	s_cselect_b32 s85, s44, s48
	s_add_u32 s36, s36, 0x40080
	s_addc_u32 s37, s37, 0
	s_add_u32 s88, s48, 0x100
	v_mov_b32_e32 v2, 0
	s_addc_u32 s89, s49, 0
	s_mov_b32 s90, -2
	v_mov_b32_e32 v3, v2
	v_mov_b64_e32 v[4:5], v[2:3]
	v_mov_b64_e32 v[6:7], v[2:3]
	v_mov_b64_e32 v[8:9], v[2:3]
	v_mov_b64_e32 v[10:11], v[2:3]
	v_mov_b64_e32 v[12:13], v[2:3]
	v_mov_b64_e32 v[14:15], v[2:3]
	v_mov_b64_e32 v[16:17], v[2:3]
	v_mov_b64_e32 v[18:19], v[2:3]
	v_mov_b64_e32 v[20:21], v[2:3]
	v_mov_b64_e32 v[22:23], v[2:3]
	v_mov_b64_e32 v[24:25], v[2:3]
	v_mov_b64_e32 v[26:27], v[2:3]
	v_mov_b64_e32 v[28:29], v[2:3]
	v_mov_b64_e32 v[30:31], v[2:3]
	v_mov_b64_e32 v[32:33], v[2:3]
	v_mov_b64_e32 v[34:35], v[2:3]
	v_mov_b64_e32 v[36:37], v[2:3]
	v_mov_b64_e32 v[38:39], v[2:3]
	v_mov_b64_e32 v[40:41], v[2:3]
	v_mov_b64_e32 v[42:43], v[2:3]
	v_mov_b64_e32 v[44:45], v[2:3]
	v_mov_b64_e32 v[46:47], v[2:3]
	v_mov_b64_e32 v[48:49], v[2:3]
	v_mov_b64_e32 v[50:51], v[2:3]
	v_mov_b64_e32 v[52:53], v[2:3]
	v_mov_b64_e32 v[54:55], v[2:3]
	v_mov_b64_e32 v[56:57], v[2:3]
	v_mov_b64_e32 v[58:59], v[2:3]
	v_mov_b64_e32 v[60:61], v[2:3]
	v_mov_b64_e32 v[62:63], v[2:3]
	v_mov_b64_e32 v[64:65], v[2:3]
	v_mov_b64_e32 v[66:67], v[2:3]
	v_mov_b64_e32 v[68:69], v[2:3]
	v_mov_b64_e32 v[70:71], v[2:3]
	v_mov_b64_e32 v[72:73], v[2:3]
	v_mov_b64_e32 v[74:75], v[2:3]
	v_mov_b64_e32 v[76:77], v[2:3]
	v_mov_b64_e32 v[78:79], v[2:3]
	v_mov_b64_e32 v[80:81], v[2:3]
	v_mov_b64_e32 v[82:83], v[2:3]
	v_mov_b64_e32 v[84:85], v[2:3]
	v_mov_b64_e32 v[86:87], v[2:3]
	v_mov_b64_e32 v[88:89], v[2:3]
	v_mov_b64_e32 v[90:91], v[2:3]
	v_mov_b64_e32 v[92:93], v[2:3]
	v_mov_b64_e32 v[94:95], v[2:3]
	v_mov_b64_e32 v[96:97], v[2:3]
	v_mov_b64_e32 v[98:99], v[2:3]
	v_mov_b64_e32 v[100:101], v[2:3]
	v_mov_b64_e32 v[102:103], v[2:3]
	v_mov_b64_e32 v[104:105], v[2:3]
	v_mov_b64_e32 v[106:107], v[2:3]
	v_mov_b64_e32 v[108:109], v[2:3]
	v_mov_b64_e32 v[110:111], v[2:3]
	v_mov_b64_e32 v[112:113], v[2:3]
	v_mov_b64_e32 v[114:115], v[2:3]
	v_mov_b64_e32 v[116:117], v[2:3]
	v_mov_b64_e32 v[118:119], v[2:3]
	v_mov_b64_e32 v[120:121], v[2:3]
	v_mov_b64_e32 v[122:123], v[2:3]
	v_mov_b64_e32 v[124:125], v[2:3]
	v_mov_b64_e32 v[126:127], v[2:3]
	v_mov_b64_e32 v[128:129], v[2:3]
	v_add_u32_e32 v0, 0x10000, v162
.LBB0_1058:
	ds_read_b128 v[164:167], v0
	ds_read_b128 v[168:171], v0 offset:1024
	ds_read_b128 v[172:175], v0 offset:2048
	ds_read_b128 v[176:179], v0 offset:3072
	ds_read_b128 v[180:183], v0 offset:16384
	ds_read_b128 v[184:187], v0 offset:17408
	ds_read_b128 v[188:191], v0 offset:18432
	ds_read_b128 v[192:195], v0 offset:19456
	s_add_u32 s48, s36, 0xfffc0080
	s_addc_u32 s49, s37, -1
	s_cmp_eq_u32 s90, 12
	s_cselect_b32 s51, s29, s49
	s_cselect_b32 s50, s39, s48
	s_cselect_b32 s49, s41, s89
	s_cselect_b32 s48, s85, s88
	v_lshl_add_u64 v[158:159], s[36:37], 0, v[138:139]
	s_add_i32 m0, s35, 0xc000
	ds_read_b128 v[200:203], v161
	ds_read_b128 v[204:207], v161 offset:1024
	ds_read_b128 v[208:211], v161 offset:2048
	ds_read_b128 v[212:215], v161 offset:3072
	ds_read_b128 v[216:219], v161 offset:4096
	ds_read_b128 v[220:223], v161 offset:5120
	ds_read_b128 v[236:239], v161 offset:6144
	ds_read_b128 v[240:243], v161 offset:7168
	global_load_lds_dwordx4 v138, s[36:37]
	v_lshl_add_u64 v[158:159], s[36:37], 0, v[140:141]
	s_add_i32 m0, s35, 0xe000
	s_nop 0
	global_load_lds_dwordx4 v140, s[36:37]
	s_waitcnt vmcnt(8)
	s_waitcnt lgkmcnt(0)
	s_barrier
	s_setprio 1
	s_waitcnt lgkmcnt(0)
	v_mfma_f32_16x16x32_bf16 v[126:129], v[164:167], v[200:203], v[126:129]
	v_mfma_f32_16x16x32_bf16 v[122:125], v[172:175], v[200:203], v[122:125]
	v_mfma_f32_16x16x32_bf16 v[110:113], v[164:167], v[208:211], v[110:113]
	v_mfma_f32_16x16x32_bf16 v[106:109], v[172:175], v[208:211], v[106:109]
	v_mfma_f32_16x16x32_bf16 v[94:97], v[164:167], v[216:219], v[94:97]
	v_mfma_f32_16x16x32_bf16 v[90:93], v[172:175], v[216:219], v[90:93]
	v_mfma_f32_16x16x32_bf16 v[78:81], v[164:167], v[236:239], v[78:81]
	v_mfma_f32_16x16x32_bf16 v[74:77], v[172:175], v[236:239], v[74:77]
	v_mfma_f32_16x16x32_bf16 v[126:129], v[168:171], v[204:207], v[126:129]
	v_mfma_f32_16x16x32_bf16 v[122:125], v[176:179], v[204:207], v[122:125]
	v_mfma_f32_16x16x32_bf16 v[110:113], v[168:171], v[212:215], v[110:113]
	v_mfma_f32_16x16x32_bf16 v[106:109], v[176:179], v[212:215], v[106:109]
	v_mfma_f32_16x16x32_bf16 v[94:97], v[168:171], v[220:223], v[94:97]
	v_mfma_f32_16x16x32_bf16 v[90:93], v[176:179], v[220:223], v[90:93]
	v_mfma_f32_16x16x32_bf16 v[78:81], v[168:171], v[240:243], v[78:81]
	v_mfma_f32_16x16x32_bf16 v[74:77], v[176:179], v[240:243], v[74:77]
	s_setprio 0
	s_setprio 1
	v_mfma_f32_16x16x32_bf16 v[118:121], v[180:183], v[200:203], v[118:121]
	v_mfma_f32_16x16x32_bf16 v[114:117], v[188:191], v[200:203], v[114:117]
	v_mfma_f32_16x16x32_bf16 v[102:105], v[180:183], v[208:211], v[102:105]
	v_mfma_f32_16x16x32_bf16 v[98:101], v[188:191], v[208:211], v[98:101]
	v_mfma_f32_16x16x32_bf16 v[86:89], v[180:183], v[216:219], v[86:89]
	v_mfma_f32_16x16x32_bf16 v[82:85], v[188:191], v[216:219], v[82:85]
	v_mfma_f32_16x16x32_bf16 v[70:73], v[180:183], v[236:239], v[70:73]
	v_mfma_f32_16x16x32_bf16 v[66:69], v[188:191], v[236:239], v[66:69]
	v_mfma_f32_16x16x32_bf16 v[118:121], v[184:187], v[204:207], v[118:121]
	v_mfma_f32_16x16x32_bf16 v[114:117], v[192:195], v[204:207], v[114:117]
	v_mfma_f32_16x16x32_bf16 v[102:105], v[184:187], v[212:215], v[102:105]
	v_mfma_f32_16x16x32_bf16 v[98:101], v[192:195], v[212:215], v[98:101]
	v_mfma_f32_16x16x32_bf16 v[86:89], v[184:187], v[220:223], v[86:89]
	v_mfma_f32_16x16x32_bf16 v[82:85], v[192:195], v[220:223], v[82:85]
	v_mfma_f32_16x16x32_bf16 v[70:73], v[184:187], v[240:243], v[70:73]
	v_mfma_f32_16x16x32_bf16 v[66:69], v[192:195], v[240:243], v[66:69]
	s_setprio 0
	s_barrier
	s_mov_b32 m0, s53
	v_lshl_add_u64 v[158:159], s[48:49], 0, v[134:135]
	s_add_u32 s92, s48, 0x40000
	ds_read_b128 v[200:203], v161 offset:16384
	ds_read_b128 v[204:207], v161 offset:17408
	ds_read_b128 v[208:211], v161 offset:18432
	ds_read_b128 v[212:215], v161 offset:19456
	ds_read_b128 v[216:219], v161 offset:20480
	ds_read_b128 v[220:223], v161 offset:21504
	ds_read_b128 v[236:239], v161 offset:22528
	ds_read_b128 v[240:243], v161 offset:23552
	global_load_lds_dwordx4 v134, s[48:49]
	v_lshl_add_u64 v[226:227], s[48:49], 0, v[130:131]
	s_mov_b32 m0, s54
	s_addc_u32 s93, s49, 0
	global_load_lds_dwordx4 v130, s[48:49]
	s_mov_b32 m0, s55
	v_lshl_add_u64 v[246:247], s[50:51], 0, v[132:133]
	global_load_lds_dwordx4 v134, s[92:93]
	s_mov_b32 m0, s56
	s_nop 0
	global_load_lds_dwordx4 v130, s[92:93]
	v_lshl_add_u64 v[244:245], s[50:51], 0, v[136:137]
	s_mov_b32 m0, s35
	s_nop 0
	global_load_lds_dwordx4 v136, s[50:51]
	s_mov_b32 m0, s57
	s_nop 0
	global_load_lds_dwordx4 v132, s[50:51]
	s_waitcnt vmcnt(8)
	s_waitcnt lgkmcnt(0)
	s_barrier
	s_setprio 1
	s_waitcnt lgkmcnt(0)
	v_mfma_f32_16x16x32_bf16 v[62:65], v[164:167], v[200:203], v[62:65]
	v_mfma_f32_16x16x32_bf16 v[58:61], v[172:175], v[200:203], v[58:61]
	v_mfma_f32_16x16x32_bf16 v[46:49], v[164:167], v[208:211], v[46:49]
	v_mfma_f32_16x16x32_bf16 v[42:45], v[172:175], v[208:211], v[42:45]
	v_mfma_f32_16x16x32_bf16 v[30:33], v[164:167], v[216:219], v[30:33]
	v_mfma_f32_16x16x32_bf16 v[26:29], v[172:175], v[216:219], v[26:29]
	v_mfma_f32_16x16x32_bf16 v[14:17], v[164:167], v[236:239], v[14:17]
	v_mfma_f32_16x16x32_bf16 v[10:13], v[172:175], v[236:239], v[10:13]
	v_mfma_f32_16x16x32_bf16 v[62:65], v[168:171], v[204:207], v[62:65]
	v_mfma_f32_16x16x32_bf16 v[58:61], v[176:179], v[204:207], v[58:61]
	v_mfma_f32_16x16x32_bf16 v[46:49], v[168:171], v[212:215], v[46:49]
	v_mfma_f32_16x16x32_bf16 v[42:45], v[176:179], v[212:215], v[42:45]
	v_mfma_f32_16x16x32_bf16 v[30:33], v[168:171], v[220:223], v[30:33]
	v_mfma_f32_16x16x32_bf16 v[26:29], v[176:179], v[220:223], v[26:29]
	v_mfma_f32_16x16x32_bf16 v[14:17], v[168:171], v[240:243], v[14:17]
	v_mfma_f32_16x16x32_bf16 v[10:13], v[176:179], v[240:243], v[10:13]
	s_setprio 0
	s_setprio 1
	v_mfma_f32_16x16x32_bf16 v[54:57], v[180:183], v[200:203], v[54:57]
	v_mfma_f32_16x16x32_bf16 v[50:53], v[188:191], v[200:203], v[50:53]
	v_mfma_f32_16x16x32_bf16 v[38:41], v[180:183], v[208:211], v[38:41]
	v_mfma_f32_16x16x32_bf16 v[34:37], v[188:191], v[208:211], v[34:37]
	v_mfma_f32_16x16x32_bf16 v[22:25], v[180:183], v[216:219], v[22:25]
	v_mfma_f32_16x16x32_bf16 v[18:21], v[188:191], v[216:219], v[18:21]
	v_mfma_f32_16x16x32_bf16 v[6:9], v[180:183], v[236:239], v[6:9]
	v_mfma_f32_16x16x32_bf16 v[2:5], v[188:191], v[236:239], v[2:5]
	v_mfma_f32_16x16x32_bf16 v[54:57], v[184:187], v[204:207], v[54:57]
	v_mfma_f32_16x16x32_bf16 v[50:53], v[192:195], v[204:207], v[50:53]
	v_mfma_f32_16x16x32_bf16 v[38:41], v[184:187], v[212:215], v[38:41]
	v_mfma_f32_16x16x32_bf16 v[34:37], v[192:195], v[212:215], v[34:37]
	v_mfma_f32_16x16x32_bf16 v[22:25], v[184:187], v[220:223], v[22:25]
	v_mfma_f32_16x16x32_bf16 v[18:21], v[192:195], v[220:223], v[18:21]
	v_mfma_f32_16x16x32_bf16 v[6:9], v[184:187], v[240:243], v[6:9]
	v_mfma_f32_16x16x32_bf16 v[2:5], v[192:195], v[240:243], v[2:5]
	s_setprio 0
	s_barrier
	ds_read_b128 v[164:167], v0 offset:32768
	ds_read_b128 v[168:171], v0 offset:33792
	ds_read_b128 v[172:175], v0 offset:34816
	ds_read_b128 v[176:179], v0 offset:35840
	ds_read_b128 v[180:183], v0 offset:49152
	ds_read_b128 v[184:187], v0 offset:50176
	ds_read_b128 v[188:191], v0 offset:51200
	ds_read_b128 v[192:195], v0 offset:52224
	s_add_u32 s50, s50, 0x40000
	s_addc_u32 s51, s51, 0
	s_mov_b32 m0, s58
	ds_read_b128 v[200:203], v161 offset:32768
	ds_read_b128 v[204:207], v161 offset:33792
	ds_read_b128 v[208:211], v161 offset:34816
	ds_read_b128 v[212:215], v161 offset:35840
	ds_read_b128 v[216:219], v161 offset:36864
	ds_read_b128 v[220:223], v161 offset:37888
	ds_read_b128 v[236:239], v161 offset:38912
	ds_read_b128 v[240:243], v161 offset:39936
	global_load_lds_dwordx4 v136, s[50:51]
	s_mov_b32 m0, s59
	s_nop 0
	global_load_lds_dwordx4 v132, s[50:51]
	s_waitcnt vmcnt(8)
	s_waitcnt lgkmcnt(0)
	s_barrier
	s_setprio 1
	s_waitcnt lgkmcnt(0)
	v_mfma_f32_16x16x32_bf16 v[126:129], v[164:167], v[200:203], v[126:129]
	v_mfma_f32_16x16x32_bf16 v[122:125], v[172:175], v[200:203], v[122:125]
	v_mfma_f32_16x16x32_bf16 v[110:113], v[164:167], v[208:211], v[110:113]
	v_mfma_f32_16x16x32_bf16 v[106:109], v[172:175], v[208:211], v[106:109]
	v_mfma_f32_16x16x32_bf16 v[94:97], v[164:167], v[216:219], v[94:97]
	v_mfma_f32_16x16x32_bf16 v[90:93], v[172:175], v[216:219], v[90:93]
	v_mfma_f32_16x16x32_bf16 v[78:81], v[164:167], v[236:239], v[78:81]
	v_mfma_f32_16x16x32_bf16 v[74:77], v[172:175], v[236:239], v[74:77]
	v_mfma_f32_16x16x32_bf16 v[126:129], v[168:171], v[204:207], v[126:129]
	v_mfma_f32_16x16x32_bf16 v[122:125], v[176:179], v[204:207], v[122:125]
	v_mfma_f32_16x16x32_bf16 v[110:113], v[168:171], v[212:215], v[110:113]
	v_mfma_f32_16x16x32_bf16 v[106:109], v[176:179], v[212:215], v[106:109]
	v_mfma_f32_16x16x32_bf16 v[94:97], v[168:171], v[220:223], v[94:97]
	v_mfma_f32_16x16x32_bf16 v[90:93], v[176:179], v[220:223], v[90:93]
	v_mfma_f32_16x16x32_bf16 v[78:81], v[168:171], v[240:243], v[78:81]
	v_mfma_f32_16x16x32_bf16 v[74:77], v[176:179], v[240:243], v[74:77]
	s_setprio 0
	s_setprio 1
	v_mfma_f32_16x16x32_bf16 v[118:121], v[180:183], v[200:203], v[118:121]
	v_mfma_f32_16x16x32_bf16 v[114:117], v[188:191], v[200:203], v[114:117]
	v_mfma_f32_16x16x32_bf16 v[102:105], v[180:183], v[208:211], v[102:105]
	v_mfma_f32_16x16x32_bf16 v[98:101], v[188:191], v[208:211], v[98:101]
	v_mfma_f32_16x16x32_bf16 v[86:89], v[180:183], v[216:219], v[86:89]
	v_mfma_f32_16x16x32_bf16 v[82:85], v[188:191], v[216:219], v[82:85]
	v_mfma_f32_16x16x32_bf16 v[70:73], v[180:183], v[236:239], v[70:73]
	v_mfma_f32_16x16x32_bf16 v[66:69], v[188:191], v[236:239], v[66:69]
	v_mfma_f32_16x16x32_bf16 v[118:121], v[184:187], v[204:207], v[118:121]
	v_mfma_f32_16x16x32_bf16 v[114:117], v[192:195], v[204:207], v[114:117]
	v_mfma_f32_16x16x32_bf16 v[102:105], v[184:187], v[212:215], v[102:105]
	v_mfma_f32_16x16x32_bf16 v[98:101], v[192:195], v[212:215], v[98:101]
	v_mfma_f32_16x16x32_bf16 v[86:89], v[184:187], v[220:223], v[86:89]
	v_mfma_f32_16x16x32_bf16 v[82:85], v[192:195], v[220:223], v[82:85]
	v_mfma_f32_16x16x32_bf16 v[70:73], v[184:187], v[240:243], v[70:73]
	v_mfma_f32_16x16x32_bf16 v[66:69], v[192:195], v[240:243], v[66:69]
	s_setprio 0
	s_barrier
	s_mov_b32 m0, s62
	v_lshl_add_u64 v[158:159], v[158:159], 0, s[18:19]
	s_add_u32 s48, s48, 0x40080
	ds_read_b128 v[200:203], v161 offset:49152
	ds_read_b128 v[204:207], v161 offset:50176
	ds_read_b128 v[208:211], v161 offset:51200
	ds_read_b128 v[212:215], v161 offset:52224
	ds_read_b128 v[216:219], v161 offset:53248
	ds_read_b128 v[220:223], v161 offset:54272
	ds_read_b128 v[236:239], v161 offset:55296
	ds_read_b128 v[240:243], v161 offset:56320
	global_load_lds_dwordx4 v[158:159], off
	v_lshl_add_u64 v[158:159], v[226:227], 0, s[18:19]
	s_mov_b32 m0, s63
	s_addc_u32 s49, s49, 0
	global_load_lds_dwordx4 v[158:159], off
	v_lshl_add_u64 v[158:159], s[48:49], 0, v[134:135]
	s_mov_b32 m0, s66
	s_nop 0
	global_load_lds_dwordx4 v134, s[48:49]
	v_lshl_add_u64 v[158:159], s[48:49], 0, v[130:131]
	s_mov_b32 m0, s67
	s_nop 0
	global_load_lds_dwordx4 v130, s[48:49]
	v_lshl_add_u64 v[158:159], v[244:245], 0, s[18:19]
	s_mov_b32 m0, s64
	s_nop 0
	global_load_lds_dwordx4 v[158:159], off
	v_lshl_add_u64 v[158:159], v[246:247], 0, s[18:19]
	s_mov_b32 m0, s65
	s_nop 0
	global_load_lds_dwordx4 v[158:159], off
	s_waitcnt vmcnt(8)
	s_waitcnt lgkmcnt(0)
	s_barrier
	s_setprio 1
	s_waitcnt lgkmcnt(0)
	v_mfma_f32_16x16x32_bf16 v[62:65], v[164:167], v[200:203], v[62:65]
	v_mfma_f32_16x16x32_bf16 v[58:61], v[172:175], v[200:203], v[58:61]
	v_mfma_f32_16x16x32_bf16 v[46:49], v[164:167], v[208:211], v[46:49]
	v_mfma_f32_16x16x32_bf16 v[42:45], v[172:175], v[208:211], v[42:45]
	v_mfma_f32_16x16x32_bf16 v[30:33], v[164:167], v[216:219], v[30:33]
	v_mfma_f32_16x16x32_bf16 v[26:29], v[172:175], v[216:219], v[26:29]
	v_mfma_f32_16x16x32_bf16 v[14:17], v[164:167], v[236:239], v[14:17]
	v_mfma_f32_16x16x32_bf16 v[10:13], v[172:175], v[236:239], v[10:13]
	v_mfma_f32_16x16x32_bf16 v[62:65], v[168:171], v[204:207], v[62:65]
	v_mfma_f32_16x16x32_bf16 v[58:61], v[176:179], v[204:207], v[58:61]
	v_mfma_f32_16x16x32_bf16 v[46:49], v[168:171], v[212:215], v[46:49]
	v_mfma_f32_16x16x32_bf16 v[42:45], v[176:179], v[212:215], v[42:45]
	v_mfma_f32_16x16x32_bf16 v[30:33], v[168:171], v[220:223], v[30:33]
	v_mfma_f32_16x16x32_bf16 v[26:29], v[176:179], v[220:223], v[26:29]
	v_mfma_f32_16x16x32_bf16 v[14:17], v[168:171], v[240:243], v[14:17]
	v_mfma_f32_16x16x32_bf16 v[10:13], v[176:179], v[240:243], v[10:13]
	s_setprio 0
	s_setprio 1
	v_mfma_f32_16x16x32_bf16 v[54:57], v[180:183], v[200:203], v[54:57]
	v_mfma_f32_16x16x32_bf16 v[50:53], v[188:191], v[200:203], v[50:53]
	v_mfma_f32_16x16x32_bf16 v[38:41], v[180:183], v[208:211], v[38:41]
	v_mfma_f32_16x16x32_bf16 v[34:37], v[188:191], v[208:211], v[34:37]
	v_mfma_f32_16x16x32_bf16 v[22:25], v[180:183], v[216:219], v[22:25]
	v_mfma_f32_16x16x32_bf16 v[18:21], v[188:191], v[216:219], v[18:21]
	v_mfma_f32_16x16x32_bf16 v[6:9], v[180:183], v[236:239], v[6:9]
	v_mfma_f32_16x16x32_bf16 v[2:5], v[188:191], v[236:239], v[2:5]
	v_mfma_f32_16x16x32_bf16 v[54:57], v[184:187], v[204:207], v[54:57]
	v_mfma_f32_16x16x32_bf16 v[50:53], v[192:195], v[204:207], v[50:53]
	v_mfma_f32_16x16x32_bf16 v[38:41], v[184:187], v[212:215], v[38:41]
	v_mfma_f32_16x16x32_bf16 v[34:37], v[192:195], v[212:215], v[34:37]
	v_mfma_f32_16x16x32_bf16 v[22:25], v[184:187], v[220:223], v[22:25]
	v_mfma_f32_16x16x32_bf16 v[18:21], v[192:195], v[220:223], v[18:21]
	v_mfma_f32_16x16x32_bf16 v[6:9], v[184:187], v[240:243], v[6:9]
	v_mfma_f32_16x16x32_bf16 v[2:5], v[192:195], v[240:243], v[2:5]
	s_setprio 0
	s_barrier
	s_add_i32 s90, s90, 2
	s_add_u32 s36, s36, 0x100
	s_addc_u32 s37, s37, 0
	s_add_u32 s88, s88, 0x100
	s_addc_u32 s89, s89, 0
	s_cmp_gt_u32 s90, 13
	s_cbranch_scc0 .LBB0_1058
	s_and_b64 vcc, exec, s[16:17]
	s_cbranch_vccz .LBB0_1061
	s_barrier
